# expert-table f32->fp4 conversion moved from the bandwidth-bound norm2 phase to the end of the peer_wq GEMM phase (idle tile round in layer 0; workgroups with 3 tiles skip it), all 8 row loads of a tab
# speedup vs baseline: 1.0011x; 1.0004x over previous
.LBB0_552:
	s_or_b64 exec, exec, s[10:11]
	v_mov_b32_e32 v2, v0
	v_readlane_b32 s0, v253, 52
	v_ashrrev_i32_e32 v3, 6, v2
	s_nop 0
	v_add_u32_e32 v40, s0, v3
	v_cmp_gt_i32_e32 vcc, s53, v40
	s_and_saveexec_b64 s[10:11], vcc
	v_readlane_b32 s76, v255, 56
	v_readlane_b32 s77, v255, 57
	s_branch .LBB0_557

.LBB0_617:
	s_mov_b32 s5, 0x8000
	v_readlane_b32 s6, v255, 49
	v_readlane_b32 s76, v255, 56
	v_mov_b32_e32 v2, v0
	v_readlane_b32 s0, v253, 52
	s_nop 0
	s_sub_i32 s0, s0, 64
	s_add_i32 s6, s6, 0xffffffc0
	s_cmp_lt_i32 s0, 0
	s_cbranch_scc1 .Lcvtx_skip
	v_ashrrev_i32_e32 v3, 6, v2
	s_nop 0
	v_add_u32_e32 v40, s0, v3
	v_cmp_gt_i32_e32 vcc, s5, v40
	s_and_saveexec_b64 s[10:11], vcc
	s_cbranch_execz .Lcvtx_done
	v_and_b32_e32 v3, 63, v2
	v_lshlrev_b32_e32 v4, 5, v3
	v_cmp_eq_u32_e64 s[0:1], 0, v3
	v_lshlrev_b32_e32 v3, 11, v2
	v_lshlrev_b32_e32 v2, 4, v2
	s_lshl_b32 s80, s76, 14
	v_and_b32_e32 v34, 0x1c000, v3
	v_mov_b32_e32 v35, v211
	v_and_b32_e32 v36, 0x70, v2
	v_mov_b32_e32 v37, v211
	s_mov_b64 s[54:55], 0
	v_lshlrev_b32_e32 v210, 2, v4
	s_branch .Lcvtx_loop
.Lcvtx_next:
	s_or_b64 exec, exec, s[34:35]
	s_mov_b32 s4, 0x40c00000
	v_div_scale_f32 v42, s[2:3], v41, v41, s4
	v_rcp_f32_e32 v43, v42
	v_div_scale_f32 v44, vcc, s4, v41, s4
	v_add_u32_e32 v40, s6, v40
	v_fma_f32 v45, -v42, v43, 1.0
	v_fmac_f32_e32 v43, v45, v43
	v_mul_f32_e32 v45, v44, v43
	v_fma_f32 v46, -v42, v45, v44
	v_fmac_f32_e32 v45, v46, v43
	v_fma_f32 v42, -v42, v45, v44
	v_div_fmas_f32 v42, v42, v43, v45
	v_div_fixup_f32 v42, v42, v41, s4
	v_cmp_lt_f32_e32 vcc, 0, v41
	s_movk_i32 s2, 0x7fff
	s_nop 0
	v_cndmask_b32_e32 v41, 0, v42, vcc
	v_mul_f32_e32 v42, v26, v41
	v_mul_f32_e32 v27, v27, v41
	v_mov_b32_e32 v26, v211
	v_cvt_scalef32_pk_fp4_f32 v26, v42, v27, 1.0
	v_mul_f32_e32 v27, v28, v41
	v_mul_f32_e32 v28, v29, v41
	v_cvt_scalef32_pk_fp4_f32 v26, v27, v28, 1.0 op_sel:[0,0,1,0]
	v_mul_f32_e32 v10, v10, v41
	v_mul_f32_e32 v11, v11, v41
	v_mov_b32_e32 v27, v211
	v_cvt_scalef32_pk_fp4_f32 v27, v10, v11, 1.0
	v_mul_f32_e32 v10, v12, v41
	v_mul_f32_e32 v11, v13, v41
	v_cvt_scalef32_pk_fp4_f32 v27, v10, v11, 1.0 op_sel:[0,0,1,0]
	v_mul_f32_e32 v2, v2, v41
	v_mul_f32_e32 v3, v3, v41
	v_cvt_scalef32_pk_fp4_f32 v27, v2, v3, 1.0 op_sel:[0,0,0,1]
	v_mul_f32_e32 v2, v4, v41
	v_mul_f32_e32 v3, v5, v41
	v_cvt_scalef32_pk_fp4_f32 v27, v2, v3, 1.0 op_sel:[0,0,1,1]
	v_mul_f32_e32 v2, v30, v41
	v_mul_f32_e32 v3, v31, v41
	v_mov_b32_e32 v28, v211
	v_cvt_scalef32_pk_fp4_f32 v28, v2, v3, 1.0
	v_mul_f32_e32 v2, v32, v41
	v_mul_f32_e32 v3, v33, v41
	v_cvt_scalef32_pk_fp4_f32 v28, v2, v3, 1.0 op_sel:[0,0,1,0]
	v_mul_f32_e32 v2, v22, v41
	v_mul_f32_e32 v3, v23, v41
	v_cvt_scalef32_pk_fp4_f32 v28, v2, v3, 1.0 op_sel:[0,0,0,1]
	v_mul_f32_e32 v2, v24, v41
	v_mul_f32_e32 v3, v25, v41
	v_cvt_scalef32_pk_fp4_f32 v28, v2, v3, 1.0 op_sel:[0,0,1,1]
	v_mul_f32_e32 v2, v14, v41
	v_mul_f32_e32 v3, v15, v41
	v_mov_b32_e32 v29, v211
	v_cvt_scalef32_pk_fp4_f32 v29, v2, v3, 1.0
	v_mul_f32_e32 v2, v16, v41
	v_mul_f32_e32 v3, v17, v41
	v_cvt_scalef32_pk_fp4_f32 v29, v2, v3, 1.0 op_sel:[0,0,1,0]
	v_mul_f32_e32 v2, v6, v41
	v_mul_f32_e32 v3, v7, v41
	v_cvt_scalef32_pk_fp4_f32 v29, v2, v3, 1.0 op_sel:[0,0,0,1]
	v_mul_f32_e32 v2, v8, v41
	v_mul_f32_e32 v3, v9, v41
	v_cvt_scalef32_pk_fp4_f32 v29, v2, v3, 1.0 op_sel:[0,0,1,1]
	v_cndmask_b32_e64 v2, v228, v229, s[50:51]
	v_mov_b32_e32 v3, v211
	v_lshl_add_u64 v[4:5], v[38:39], 0, v[34:35]
	v_mul_f32_e32 v18, v18, v41
	v_mul_f32_e32 v19, v19, v41
	v_lshl_add_u64 v[2:3], s[96:97], 0, v[2:3]
	v_lshlrev_b64 v[4:5], 7, v[4:5]
	v_cvt_scalef32_pk_fp4_f32 v26, v18, v19, 1.0 op_sel:[0,0,0,1]
	v_mul_f32_e32 v18, v20, v41
	v_mul_f32_e32 v19, v21, v41
	v_lshl_add_u64 v[2:3], v[2:3], 0, v[4:5]
	v_cmp_lt_i32_e32 vcc, s2, v40
	v_cvt_scalef32_pk_fp4_f32 v26, v18, v19, 1.0 op_sel:[0,0,1,1]
	v_lshl_add_u64 v[2:3], v[2:3], 0, v[36:37]
	s_or_b64 s[54:55], vcc, s[54:55]
	global_store_dwordx4 v[2:3], v[26:29], off
	s_andn2_b64 exec, exec, s[54:55]
	s_cbranch_execz .Lcvtx_done
.Lcvtx_loop:
	s_movk_i32 s2, 0x4000
	v_cmp_gt_i32_e64 s[50:51], s2, v40
	v_add_u32_e32 v2, 0xffffc000, v40
	v_mov_b32_e32 v3, s15
	v_cndmask_b32_e64 v38, v2, v40, s[50:51]
	v_mov_b32_e32 v2, s17
	v_cndmask_b32_e64 v3, v2, v3, s[50:51]
	v_mov_b32_e32 v2, s16
	v_mov_b32_e32 v4, s14
	v_ashrrev_i32_e32 v39, 31, v38
	v_cndmask_b32_e64 v2, v2, v4, s[50:51]
	v_lshl_add_u64 v[4:5], v[38:39], 0, s[80:81]
	v_lshlrev_b64 v[4:5], 13, v[4:5]
	v_lshl_add_u64 v[2:3], v[2:3], 0, v[4:5]
	v_lshl_add_u64 v[30:31], v[2:3], 0, v[210:211]
	global_load_dwordx4 v[2:5], v[30:31], off offset:48
	global_load_dwordx4 v[10:13], v[30:31], off offset:32
	global_load_dwordx4 v[18:21], v[30:31], off offset:16
	global_load_dwordx4 v[26:29], v[30:31], off
	global_load_dwordx4 v[6:9], v[30:31], off offset:112
	global_load_dwordx4 v[14:17], v[30:31], off offset:96
	global_load_dwordx4 v[22:25], v[30:31], off offset:80
	global_load_dwordx4 v[30:33], v[30:31], off offset:64
	s_waitcnt vmcnt(7)
	v_max_f32_e64 v50, |v4|, |v4|
	s_waitcnt vmcnt(5)
	v_max_f32_e64 v49, |v20|, |v20|
	s_waitcnt vmcnt(4)
	v_max_f32_e64 v47, |v29|, |v29|
	v_max_f32_e64 v48, |v28|, |v28|
	v_max_f32_e32 v47, v48, v47
	v_max_f32_e64 v48, |v21|, |v21|
	v_max_f32_e32 v48, v49, v48
	v_max3_f32 v47, |v26|, |v27|, v47
	v_max3_f32 v48, |v18|, |v19|, v48
	v_max3_f32 v47, v47, 0, v48
	v_max_f32_e64 v48, |v13|, |v13|
	v_max_f32_e64 v49, |v12|, |v12|
	v_max_f32_e32 v48, v49, v48
	v_max_f32_e64 v49, |v5|, |v5|
	v_max_f32_e32 v49, v50, v49
	v_max3_f32 v48, |v10|, |v11|, v48
	v_max3_f32 v49, |v2|, |v3|, v49
	v_max3_f32 v41, v47, v48, v49
	s_waitcnt vmcnt(1)
	v_max_f32_e64 v44, |v24|, |v24|
	s_waitcnt vmcnt(0)
	v_max_f32_e64 v42, |v33|, |v33|
	v_max_f32_e64 v43, |v32|, |v32|
	v_max_f32_e32 v42, v43, v42
	v_max_f32_e64 v43, |v25|, |v25|
	v_max_f32_e32 v43, v44, v43
	v_max3_f32 v42, |v30|, |v31|, v42
	v_max3_f32 v43, |v22|, |v23|, v43
	v_max3_f32 v41, v41, v42, v43
	v_max_f32_e64 v42, |v17|, |v17|
	v_max_f32_e64 v43, |v16|, |v16|
	v_max_f32_e32 v42, v43, v42
	v_max_f32_e64 v43, |v9|, |v9|
	v_max_f32_e64 v44, |v8|, |v8|
	v_max_f32_e32 v43, v44, v43
	v_max3_f32 v42, |v14|, |v15|, v42
	v_max3_f32 v43, |v6|, |v7|, v43
	v_max3_f32 v41, v41, v42, v43
	ds_swizzle_b32 v42, v41 offset:swizzle(SWAP,1)
	s_waitcnt lgkmcnt(0)
	v_max_f32_e32 v42, v42, v42
	v_max_f32_e32 v41, v41, v42
	ds_swizzle_b32 v42, v41 offset:swizzle(SWAP,2)
	s_waitcnt lgkmcnt(0)
	v_max_f32_e32 v42, v42, v42
	v_max_f32_e32 v41, v41, v42
	ds_swizzle_b32 v42, v41 offset:swizzle(SWAP,4)
	s_waitcnt lgkmcnt(0)
	v_max_f32_e32 v42, v42, v42
	v_max_f32_e32 v41, v41, v42
	ds_swizzle_b32 v42, v41 offset:swizzle(SWAP,8)
	s_waitcnt lgkmcnt(0)
	v_max_f32_e32 v42, v42, v42
	v_max_f32_e32 v41, v41, v42
	ds_swizzle_b32 v42, v41 offset:swizzle(SWAP,16)
	s_waitcnt lgkmcnt(0)
	v_max_f32_e32 v42, v42, v42
	v_max_f32_e32 v41, v41, v42
	v_mov_b32_e32 v42, v41
	s_nop 1
	v_permlane32_swap_b32_e32 v41, v42
	v_max_f32_e32 v42, v42, v42
	v_max_f32_e32 v41, v41, v41
	v_max_f32_e32 v41, v41, v42
	s_and_saveexec_b64 s[34:35], s[0:1]
	s_cbranch_execz .Lcvtx_next
	v_mov_b32_e32 v42, 0x27400000
	v_cndmask_b32_e64 v42, v252, v42, s[50:51]
	v_mov_b32_e32 v43, v211
	v_lshl_add_u64 v[42:43], s[96:97], 0, v[42:43]
	v_mul_f32_e32 v44, 0x3e2aaaab, v41
	v_lshl_add_u64 v[42:43], v[38:39], 2, v[42:43]
	global_store_dword v[42:43], v44, off
	s_branch .Lcvtx_next
.Lcvtx_done:
	s_or_b64 exec, exec, s[10:11]
.Lcvtx_skip:
	s_waitcnt vmcnt(0)
	s_waitcnt vmcnt(0) lgkmcnt(0)
	s_barrier
	s_and_saveexec_b64 s[0:1], s[44:45]
	v_readlane_b32 s84, v255, 52
	v_readlane_b32 s85, v255, 53
	s_cbranch_execz .LBB0_665
	v_readlane_b32 s2, v255, 29
	s_waitcnt vmcnt(0) expcnt(0) lgkmcnt(0)
	s_nop 0
	v_mov_b32_e32 v2, s2
	ds_read_b32 v4, v2
	v_readlane_b32 s2, v255, 30
	s_waitcnt lgkmcnt(0)
	v_cmp_ne_u32_e32 vcc, 0, v4
	v_mov_b32_e32 v2, s2
	ds_read_b32 v2, v2
	s_cbranch_vccnz .LBB0_633
	v_readlane_b32 s4, v253, 16
	v_readlane_b32 s5, v253, 17
	s_load_dwordx2 s[2:3], s[4:5], 0x4
	s_waitcnt lgkmcnt(0)
	s_mul_i32 s2, s2, s86
	s_mul_i32 s2, s2, s3
	s_mov_b32 s3, 1
	s_branch .LBB0_621
